# epilogue de-serialisation: MoE down-proj epilogue (both layers) no longer waits for the previous row group's scatter stores (7 vmcnt(0) per unit replaced by one)
# baseline (speedup 1.0000x reference)
; __device__ __forceinline__ unsigned cvt_pk_bf16(float lo, float hi) { unsigned r; asm volatile("v_cvt_pk_bf16_f32 %0, %1, %2" : "=v"(r) : "v"(lo), "v"(hi)); return r; }
;     __device__ __forceinline__ void operator()(const f32x4 (&acc)[2][2][4][2], const Unit& u, int wr, int wc, int fr, int fq) const {
;     ...
;             for (int m = 0; m < 4; ++m) { const int r = u.pm * 256 + ai * HALF + wr * 64 + m * 16 + fr, rc = r < u.cnt ? r : u.cnt - 1; pr[ai][m] = pair_of[rc]; gwv[ai][m] = gate_of[rc]; }
; #pragma unroll
;         for (int ai = 0; ai < 2; ++ai)
; #pragma unroll
;             for (int m = 0; m < 4; ++m) { const int r = u.pm * 256 + ai * HALF + wr * 64 + m * 16 + fr;
;                 if (r < u.cnt) { const float gw = gwv[ai][m]; bf16* rowp = Y + (size_t)pr[ai][m] * 1024 + col0;
; #pragma unroll
;                     for (int bj = 0; bj < 2; ++bj) { const f32x4 v0 = (acc[ai][bj][m][0] + bv[bj][0]) * gw, v1 = (acc[ai][bj][m][1] + bv[bj][1]) * gw;
;                         u32x4 w; w.x = cvt_pk_bf16(v0[0], v0[1]); w.y = cvt_pk_bf16(v0[2], v0[3]); w.z = cvt_pk_bf16(v1[0], v1[1]); w.w = cvt_pk_bf16(v1[2], v1[3]);
;                         *(u32x4*)(rowp + bj * HALF) = w; } } }
.LBB0_1591:
	s_or_b64 exec, exec, s[18:19]
	s_waitcnt vmcnt(0)
	s_nop 0
	v_add_u32_e32 v114, s22, v193
	v_cmp_lt_i32_e32 vcc, v114, v159
	s_and_saveexec_b64 s[16:17], vcc
	s_cbranch_execz .LBB0_1593
	v_ashrrev_i32_e32 v195, 31, v194
	v_lshlrev_b64 v[114:115], 11, v[194:195]
	v_pk_add_f32 v[112:113], v[112:113], v[144:145]
	v_pk_add_f32 v[110:111], v[110:111], v[142:143]
	v_pk_add_f32 v[108:109], v[108:109], v[140:141]
	v_pk_add_f32 v[106:107], v[106:107], v[138:139]
	v_lshl_add_u64 v[114:115], v[168:169], 0, v[114:115]
	v_pk_mul_f32 v[112:113], v[112:113], v[192:193] op_sel_hi:[1,0]
	v_pk_mul_f32 v[110:111], v[110:111], v[192:193] op_sel_hi:[1,0]
	v_pk_mul_f32 v[116:117], v[108:109], v[192:193] op_sel_hi:[1,0]
	v_pk_mul_f32 v[108:109], v[106:107], v[192:193] op_sel_hi:[1,0]
	v_cvt_pk_bf16_f32 v106, v110, v111
	v_cvt_pk_bf16_f32 v107, v112, v113
	v_pk_add_f32 v[100:101], v[100:101], v[132:133]
	v_pk_add_f32 v[98:99], v[98:99], v[130:131]
	v_cvt_pk_bf16_f32 v108, v108, v109
	v_cvt_pk_bf16_f32 v109, v116, v117
	global_store_dwordx4 v[114:115], v[106:109], off
	v_pk_add_f32 v[104:105], v[104:105], v[136:137]
	v_pk_add_f32 v[102:103], v[102:103], v[134:135]
	v_pk_mul_f32 v[106:107], v[100:101], v[192:193] op_sel_hi:[1,0]
	v_pk_mul_f32 v[100:101], v[98:99], v[192:193] op_sel_hi:[1,0]
	v_pk_mul_f32 v[104:105], v[104:105], v[192:193] op_sel_hi:[1,0]
	v_pk_mul_f32 v[102:103], v[102:103], v[192:193] op_sel_hi:[1,0]
	s_nop 0
	v_cvt_pk_bf16_f32 v98, v102, v103
	v_cvt_pk_bf16_f32 v99, v104, v105
	v_cvt_pk_bf16_f32 v100, v100, v101
	v_cvt_pk_bf16_f32 v101, v106, v107
	global_store_dwordx4 v[114:115], v[98:101], off offset:256
.LBB0_1593:
	s_or_b64 exec, exec, s[16:17]
	s_nop 0
	v_add_u32_e32 v98, s22, v198
	v_cmp_lt_i32_e32 vcc, v98, v159
	s_and_saveexec_b64 s[16:17], vcc
	s_cbranch_execz .LBB0_1595
	v_ashrrev_i32_e32 v191, 31, v190
	v_lshlrev_b64 v[98:99], 11, v[190:191]
	v_pk_add_f32 v[96:97], v[96:97], v[144:145]
	v_pk_add_f32 v[94:95], v[94:95], v[142:143]
	v_pk_add_f32 v[92:93], v[92:93], v[140:141]
	v_pk_add_f32 v[90:91], v[90:91], v[138:139]
	v_lshl_add_u64 v[98:99], v[168:169], 0, v[98:99]
	v_pk_mul_f32 v[96:97], v[96:97], v[188:189] op_sel_hi:[1,0]
	v_pk_mul_f32 v[94:95], v[94:95], v[188:189] op_sel_hi:[1,0]
	v_pk_mul_f32 v[100:101], v[92:93], v[188:189] op_sel_hi:[1,0]
	v_pk_mul_f32 v[92:93], v[90:91], v[188:189] op_sel_hi:[1,0]
	v_cvt_pk_bf16_f32 v90, v94, v95
	v_cvt_pk_bf16_f32 v91, v96, v97
	v_pk_add_f32 v[84:85], v[84:85], v[132:133]
	v_pk_add_f32 v[82:83], v[82:83], v[130:131]
	v_cvt_pk_bf16_f32 v92, v92, v93
	v_cvt_pk_bf16_f32 v93, v100, v101
	global_store_dwordx4 v[98:99], v[90:93], off
	v_pk_add_f32 v[88:89], v[88:89], v[136:137]
	v_pk_add_f32 v[86:87], v[86:87], v[134:135]
	v_pk_mul_f32 v[90:91], v[84:85], v[188:189] op_sel_hi:[1,0]
	v_pk_mul_f32 v[84:85], v[82:83], v[188:189] op_sel_hi:[1,0]
	v_pk_mul_f32 v[88:89], v[88:89], v[188:189] op_sel_hi:[1,0]
	v_pk_mul_f32 v[86:87], v[86:87], v[188:189] op_sel_hi:[1,0]
	s_nop 0
	v_cvt_pk_bf16_f32 v82, v86, v87
	v_cvt_pk_bf16_f32 v83, v88, v89
	v_cvt_pk_bf16_f32 v84, v84, v85
	v_cvt_pk_bf16_f32 v85, v90, v91
	global_store_dwordx4 v[98:99], v[82:85], off offset:256
.LBB0_1595:
	s_or_b64 exec, exec, s[16:17]
	s_nop 0
	v_add_u32_e32 v82, s22, v199
	v_cmp_lt_i32_e32 vcc, v82, v159
	s_and_saveexec_b64 s[16:17], vcc
	s_cbranch_execz .LBB0_1601
	v_ashrrev_i32_e32 v187, 31, v186
	v_lshlrev_b64 v[82:83], 11, v[186:187]
	v_pk_add_f32 v[80:81], v[80:81], v[144:145]
	v_pk_add_f32 v[78:79], v[78:79], v[142:143]
	v_pk_add_f32 v[76:77], v[76:77], v[140:141]
	v_pk_add_f32 v[74:75], v[74:75], v[138:139]
	v_lshl_add_u64 v[82:83], v[168:169], 0, v[82:83]
	v_pk_mul_f32 v[80:81], v[80:81], v[180:181] op_sel_hi:[1,0]
	v_pk_mul_f32 v[78:79], v[78:79], v[180:181] op_sel_hi:[1,0]
	v_pk_mul_f32 v[84:85], v[76:77], v[180:181] op_sel_hi:[1,0]
	v_pk_mul_f32 v[76:77], v[74:75], v[180:181] op_sel_hi:[1,0]
	v_cvt_pk_bf16_f32 v74, v78, v79
	v_cvt_pk_bf16_f32 v75, v80, v81
	v_pk_add_f32 v[68:69], v[68:69], v[132:133]
	v_pk_add_f32 v[66:67], v[66:67], v[130:131]
	v_cvt_pk_bf16_f32 v76, v76, v77
	v_cvt_pk_bf16_f32 v77, v84, v85
	global_store_dwordx4 v[82:83], v[74:77], off
	v_pk_add_f32 v[72:73], v[72:73], v[136:137]
	v_pk_add_f32 v[70:71], v[70:71], v[134:135]
	v_pk_mul_f32 v[74:75], v[68:69], v[180:181] op_sel_hi:[1,0]
	v_pk_mul_f32 v[68:69], v[66:67], v[180:181] op_sel_hi:[1,0]
	v_pk_mul_f32 v[72:73], v[72:73], v[180:181] op_sel_hi:[1,0]
	v_pk_mul_f32 v[70:71], v[70:71], v[180:181] op_sel_hi:[1,0]
	s_nop 0
	v_cvt_pk_bf16_f32 v66, v70, v71
	v_cvt_pk_bf16_f32 v67, v72, v73
	v_cvt_pk_bf16_f32 v68, v68, v69
	v_cvt_pk_bf16_f32 v69, v74, v75
	global_store_dwordx4 v[82:83], v[66:69], off offset:256
	s_or_b64 exec, exec, s[16:17]
	v_cmp_lt_i32_e32 vcc, v179, v159
	s_and_saveexec_b64 s[16:17], vcc
	s_cbranch_execnz .LBB0_1602

; __device__ __forceinline__ unsigned cvt_pk_bf16(float lo, float hi) { unsigned r; asm volatile("v_cvt_pk_bf16_f32 %0, %1, %2" : "=v"(r) : "v"(lo), "v"(hi)); return r; }
;     __device__ __forceinline__ void operator()(const f32x4 (&acc)[2][2][4][2], const Unit& u, int wr, int wc, int fr, int fq) const {
;     ...
;             for (int m = 0; m < 4; ++m) { const int r = u.pm * 256 + ai * HALF + wr * 64 + m * 16 + fr;
;                 if (r < u.cnt) { const float gw = gwv[ai][m]; bf16* rowp = Y + (size_t)pr[ai][m] * 1024 + col0;
; #pragma unroll
;                     for (int bj = 0; bj < 2; ++bj) { const f32x4 v0 = (acc[ai][bj][m][0] + bv[bj][0]) * gw, v1 = (acc[ai][bj][m][1] + bv[bj][1]) * gw;
;                         u32x4 w; w.x = cvt_pk_bf16(v0[0], v0[1]); w.y = cvt_pk_bf16(v0[2], v0[3]); w.z = cvt_pk_bf16(v1[0], v1[1]); w.w = cvt_pk_bf16(v1[2], v1[3]);
;                         *(u32x4*)(rowp + bj * HALF) = w; } } }
.LBB0_1598:
	v_ashrrev_i32_e32 v177, 31, v176
	v_lshlrev_b64 v[50:51], 11, v[176:177]
	v_pk_add_f32 v[48:49], v[48:49], v[144:145]
	v_pk_add_f32 v[46:47], v[46:47], v[142:143]
	v_pk_add_f32 v[44:45], v[44:45], v[140:141]
	v_pk_add_f32 v[42:43], v[42:43], v[138:139]
	v_lshl_add_u64 v[50:51], v[168:169], 0, v[50:51]
	v_pk_mul_f32 v[48:49], v[48:49], v[172:173] op_sel_hi:[1,0]
	v_pk_mul_f32 v[46:47], v[46:47], v[172:173] op_sel_hi:[1,0]
	v_pk_mul_f32 v[52:53], v[44:45], v[172:173] op_sel_hi:[1,0]
	v_pk_mul_f32 v[44:45], v[42:43], v[172:173] op_sel_hi:[1,0]
	v_cvt_pk_bf16_f32 v42, v46, v47
	v_cvt_pk_bf16_f32 v43, v48, v49
	v_pk_add_f32 v[36:37], v[36:37], v[132:133]
	v_pk_add_f32 v[34:35], v[34:35], v[130:131]
	v_cvt_pk_bf16_f32 v44, v44, v45
	v_cvt_pk_bf16_f32 v45, v52, v53
	global_store_dwordx4 v[50:51], v[42:45], off
	v_pk_add_f32 v[40:41], v[40:41], v[136:137]
	v_pk_add_f32 v[38:39], v[38:39], v[134:135]
	v_pk_mul_f32 v[42:43], v[36:37], v[172:173] op_sel_hi:[1,0]
	v_pk_mul_f32 v[36:37], v[34:35], v[172:173] op_sel_hi:[1,0]
	v_pk_mul_f32 v[40:41], v[40:41], v[172:173] op_sel_hi:[1,0]
	v_pk_mul_f32 v[38:39], v[38:39], v[172:173] op_sel_hi:[1,0]
	s_nop 0
	v_cvt_pk_bf16_f32 v34, v38, v39
	v_cvt_pk_bf16_f32 v35, v40, v41
	v_cvt_pk_bf16_f32 v36, v36, v37
	v_cvt_pk_bf16_f32 v37, v42, v43
	global_store_dwordx4 v[50:51], v[34:37], off offset:256
	s_or_b64 exec, exec, s[16:17]
	v_cmp_lt_i32_e32 vcc, v171, v159
	s_and_saveexec_b64 s[16:17], vcc
	s_cbranch_execnz .LBB0_1604

; __device__ __forceinline__ unsigned cvt_pk_bf16(float lo, float hi) { unsigned r; asm volatile("v_cvt_pk_bf16_f32 %0, %1, %2" : "=v"(r) : "v"(lo), "v"(hi)); return r; }
;     __device__ __forceinline__ void operator()(const f32x4 (&acc)[2][2][4][2], const Unit& u, int wr, int wc, int fr, int fq) const {
;     ...
;             for (int m = 0; m < 4; ++m) { const int r = u.pm * 256 + ai * HALF + wr * 64 + m * 16 + fr;
;                 if (r < u.cnt) { const float gw = gwv[ai][m]; bf16* rowp = Y + (size_t)pr[ai][m] * 1024 + col0;
; #pragma unroll
;                     for (int bj = 0; bj < 2; ++bj) { const f32x4 v0 = (acc[ai][bj][m][0] + bv[bj][0]) * gw, v1 = (acc[ai][bj][m][1] + bv[bj][1]) * gw;
;                         u32x4 w; w.x = cvt_pk_bf16(v0[0], v0[1]); w.y = cvt_pk_bf16(v0[2], v0[3]); w.z = cvt_pk_bf16(v1[0], v1[1]); w.w = cvt_pk_bf16(v1[2], v1[3]);
;                         *(u32x4*)(rowp + bj * HALF) = w; } } }
.LBB0_1600:
	v_ashrrev_i32_e32 v167, 31, v166
	v_lshlrev_b64 v[18:19], 11, v[166:167]
	v_pk_add_f32 v[16:17], v[16:17], v[144:145]
	v_pk_add_f32 v[14:15], v[14:15], v[142:143]
	v_pk_add_f32 v[12:13], v[12:13], v[140:141]
	v_pk_add_f32 v[10:11], v[10:11], v[138:139]
	v_lshl_add_u64 v[18:19], v[168:169], 0, v[18:19]
	v_pk_mul_f32 v[16:17], v[16:17], v[158:159] op_sel_hi:[1,0]
	v_pk_mul_f32 v[14:15], v[14:15], v[158:159] op_sel_hi:[1,0]
	v_pk_mul_f32 v[20:21], v[12:13], v[158:159] op_sel_hi:[1,0]
	v_pk_mul_f32 v[12:13], v[10:11], v[158:159] op_sel_hi:[1,0]
	v_cvt_pk_bf16_f32 v10, v14, v15
	v_cvt_pk_bf16_f32 v11, v16, v17
	v_pk_add_f32 v[4:5], v[4:5], v[132:133]
	v_pk_add_f32 v[2:3], v[2:3], v[130:131]
	v_cvt_pk_bf16_f32 v12, v12, v13
	v_cvt_pk_bf16_f32 v13, v20, v21
	global_store_dwordx4 v[18:19], v[10:13], off
	v_pk_add_f32 v[8:9], v[8:9], v[136:137]
	v_pk_add_f32 v[6:7], v[6:7], v[134:135]
	v_pk_mul_f32 v[10:11], v[4:5], v[158:159] op_sel_hi:[1,0]
	v_pk_mul_f32 v[4:5], v[2:3], v[158:159] op_sel_hi:[1,0]
	v_pk_mul_f32 v[8:9], v[8:9], v[158:159] op_sel_hi:[1,0]
	v_pk_mul_f32 v[6:7], v[6:7], v[158:159] op_sel_hi:[1,0]
	s_nop 0
	v_cvt_pk_bf16_f32 v2, v6, v7
	v_cvt_pk_bf16_f32 v3, v8, v9
	v_cvt_pk_bf16_f32 v4, v4, v5
	v_cvt_pk_bf16_f32 v5, v10, v11
	global_store_dwordx4 v[18:19], v[2:5], off offset:256
	s_or_b64 exec, exec, s[16:17]
	s_andn2_b64 vcc, exec, s[4:5]
	s_mov_b64 s[4:5], -1
	s_cbranch_vccnz .LBB0_1580
	s_branch .LBB0_1606

; __device__ __forceinline__ unsigned cvt_pk_bf16(float lo, float hi) { unsigned r; asm volatile("v_cvt_pk_bf16_f32 %0, %1, %2" : "=v"(r) : "v"(lo), "v"(hi)); return r; }
;     __device__ __forceinline__ void operator()(const f32x4 (&acc)[2][2][4][2], const Unit& u, int wr, int wc, int fr, int fq) const {
;     ...
;             for (int m = 0; m < 4; ++m) { const int r = u.pm * 256 + ai * HALF + wr * 64 + m * 16 + fr;
;                 if (r < u.cnt) { const float gw = gwv[ai][m]; bf16* rowp = Y + (size_t)pr[ai][m] * 1024 + col0;
; #pragma unroll
;                     for (int bj = 0; bj < 2; ++bj) { const f32x4 v0 = (acc[ai][bj][m][0] + bv[bj][0]) * gw, v1 = (acc[ai][bj][m][1] + bv[bj][1]) * gw;
;                         u32x4 w; w.x = cvt_pk_bf16(v0[0], v0[1]); w.y = cvt_pk_bf16(v0[2], v0[3]); w.z = cvt_pk_bf16(v1[0], v1[1]); w.w = cvt_pk_bf16(v1[2], v1[3]);
;                         *(u32x4*)(rowp + bj * HALF) = w; } } }
.LBB0_1602:
	v_ashrrev_i32_e32 v179, 31, v178
	v_lshlrev_b64 v[66:67], 11, v[178:179]
	v_pk_add_f32 v[64:65], v[64:65], v[144:145]
	v_pk_add_f32 v[62:63], v[62:63], v[142:143]
	v_pk_add_f32 v[60:61], v[60:61], v[140:141]
	v_pk_add_f32 v[58:59], v[58:59], v[138:139]
	v_lshl_add_u64 v[66:67], v[168:169], 0, v[66:67]
	v_pk_mul_f32 v[64:65], v[64:65], v[174:175] op_sel_hi:[1,0]
	v_pk_mul_f32 v[62:63], v[62:63], v[174:175] op_sel_hi:[1,0]
	v_pk_mul_f32 v[68:69], v[60:61], v[174:175] op_sel_hi:[1,0]
	v_pk_mul_f32 v[60:61], v[58:59], v[174:175] op_sel_hi:[1,0]
	v_cvt_pk_bf16_f32 v58, v62, v63
	v_cvt_pk_bf16_f32 v59, v64, v65
	v_pk_add_f32 v[52:53], v[52:53], v[132:133]
	v_pk_add_f32 v[50:51], v[50:51], v[130:131]
	v_cvt_pk_bf16_f32 v60, v60, v61
	v_cvt_pk_bf16_f32 v61, v68, v69
	global_store_dwordx4 v[66:67], v[58:61], off
	v_pk_add_f32 v[56:57], v[56:57], v[136:137]
	v_pk_add_f32 v[54:55], v[54:55], v[134:135]
	v_pk_mul_f32 v[58:59], v[52:53], v[174:175] op_sel_hi:[1,0]
	v_pk_mul_f32 v[52:53], v[50:51], v[174:175] op_sel_hi:[1,0]
	v_pk_mul_f32 v[56:57], v[56:57], v[174:175] op_sel_hi:[1,0]
	v_pk_mul_f32 v[54:55], v[54:55], v[174:175] op_sel_hi:[1,0]
	s_nop 0
	v_cvt_pk_bf16_f32 v50, v54, v55
	v_cvt_pk_bf16_f32 v51, v56, v57
	v_cvt_pk_bf16_f32 v52, v52, v53
	v_cvt_pk_bf16_f32 v53, v58, v59
	global_store_dwordx4 v[66:67], v[50:53], off offset:256
	s_or_b64 exec, exec, s[16:17]
	v_cmp_lt_i32_e32 vcc, v177, v159
	s_and_saveexec_b64 s[16:17], vcc
	s_cbranch_execnz .LBB0_1598

; __device__ __forceinline__ unsigned cvt_pk_bf16(float lo, float hi) { unsigned r; asm volatile("v_cvt_pk_bf16_f32 %0, %1, %2" : "=v"(r) : "v"(lo), "v"(hi)); return r; }
;     __device__ __forceinline__ void operator()(const f32x4 (&acc)[2][2][4][2], const Unit& u, int wr, int wc, int fr, int fq) const {
;     ...
;             for (int m = 0; m < 4; ++m) { const int r = u.pm * 256 + ai * HALF + wr * 64 + m * 16 + fr;
;                 if (r < u.cnt) { const float gw = gwv[ai][m]; bf16* rowp = Y + (size_t)pr[ai][m] * 1024 + col0;
; #pragma unroll
;                     for (int bj = 0; bj < 2; ++bj) { const f32x4 v0 = (acc[ai][bj][m][0] + bv[bj][0]) * gw, v1 = (acc[ai][bj][m][1] + bv[bj][1]) * gw;
;                         u32x4 w; w.x = cvt_pk_bf16(v0[0], v0[1]); w.y = cvt_pk_bf16(v0[2], v0[3]); w.z = cvt_pk_bf16(v1[0], v1[1]); w.w = cvt_pk_bf16(v1[2], v1[3]);
;                         *(u32x4*)(rowp + bj * HALF) = w; } } }
.LBB0_1604:
	v_ashrrev_i32_e32 v171, 31, v170
	v_lshlrev_b64 v[34:35], 11, v[170:171]
	v_pk_add_f32 v[32:33], v[32:33], v[144:145]
	v_pk_add_f32 v[30:31], v[30:31], v[142:143]
	v_pk_add_f32 v[28:29], v[28:29], v[140:141]
	v_pk_add_f32 v[26:27], v[26:27], v[138:139]
	v_lshl_add_u64 v[34:35], v[168:169], 0, v[34:35]
	v_pk_mul_f32 v[32:33], v[32:33], v[164:165] op_sel_hi:[1,0]
	v_pk_mul_f32 v[30:31], v[30:31], v[164:165] op_sel_hi:[1,0]
	v_pk_mul_f32 v[36:37], v[28:29], v[164:165] op_sel_hi:[1,0]
	v_pk_mul_f32 v[28:29], v[26:27], v[164:165] op_sel_hi:[1,0]
	v_cvt_pk_bf16_f32 v26, v30, v31
	v_cvt_pk_bf16_f32 v27, v32, v33
	v_pk_add_f32 v[20:21], v[20:21], v[132:133]
	v_pk_add_f32 v[18:19], v[18:19], v[130:131]
	v_cvt_pk_bf16_f32 v28, v28, v29
	v_cvt_pk_bf16_f32 v29, v36, v37
	global_store_dwordx4 v[34:35], v[26:29], off
	v_pk_add_f32 v[24:25], v[24:25], v[136:137]
	v_pk_add_f32 v[22:23], v[22:23], v[134:135]
	v_pk_mul_f32 v[26:27], v[20:21], v[164:165] op_sel_hi:[1,0]
	v_pk_mul_f32 v[20:21], v[18:19], v[164:165] op_sel_hi:[1,0]
	v_pk_mul_f32 v[24:25], v[24:25], v[164:165] op_sel_hi:[1,0]
	v_pk_mul_f32 v[22:23], v[22:23], v[164:165] op_sel_hi:[1,0]
	s_nop 0
	v_cvt_pk_bf16_f32 v18, v22, v23
	v_cvt_pk_bf16_f32 v19, v24, v25
	v_cvt_pk_bf16_f32 v20, v20, v21
	v_cvt_pk_bf16_f32 v21, v26, v27
	global_store_dwordx4 v[34:35], v[18:21], off offset:256
	s_or_b64 exec, exec, s[16:17]
	v_cmp_lt_i32_e32 vcc, v167, v159
	s_and_saveexec_b64 s[16:17], vcc
	s_cbranch_execnz .LBB0_1600

; __device__ __forceinline__ unsigned cvt_pk_bf16(float lo, float hi) { unsigned r; asm volatile("v_cvt_pk_bf16_f32 %0, %1, %2" : "=v"(r) : "v"(lo), "v"(hi)); return r; }
;     __device__ __forceinline__ void operator()(const f32x4 (&acc)[2][2][4][2], const Unit& u, int wr, int wc, int fr, int fq) const {
;     ...
;             for (int m = 0; m < 4; ++m) { const int r = u.pm * 256 + ai * HALF + wr * 64 + m * 16 + fr, rc = r < u.cnt ? r : u.cnt - 1; pr[ai][m] = pair_of[rc]; gwv[ai][m] = gate_of[rc]; }
; #pragma unroll
;         for (int ai = 0; ai < 2; ++ai)
; #pragma unroll
;             for (int m = 0; m < 4; ++m) { const int r = u.pm * 256 + ai * HALF + wr * 64 + m * 16 + fr;
;                 if (r < u.cnt) { const float gw = gwv[ai][m]; bf16* rowp = Y + (size_t)pr[ai][m] * 1024 + col0;
; #pragma unroll
;                     for (int bj = 0; bj < 2; ++bj) { const f32x4 v0 = (acc[ai][bj][m][0] + bv[bj][0]) * gw, v1 = (acc[ai][bj][m][1] + bv[bj][1]) * gw;
;                         u32x4 w; w.x = cvt_pk_bf16(v0[0], v0[1]); w.y = cvt_pk_bf16(v0[2], v0[3]); w.z = cvt_pk_bf16(v1[0], v1[1]); w.w = cvt_pk_bf16(v1[2], v1[3]);
;                         *(u32x4*)(rowp + bj * HALF) = w; } } }
.LBB0_2453:
	s_or_b64 exec, exec, s[20:21]
	s_waitcnt vmcnt(0)
	s_nop 0
	v_add_u32_e32 v114, s24, v181
	v_cmp_lt_i32_e32 vcc, v114, v159
	s_and_saveexec_b64 s[18:19], vcc
	s_cbranch_execz .LBB0_2455
	v_ashrrev_i32_e32 v191, 31, v190
	v_lshlrev_b64 v[114:115], 11, v[190:191]
	v_pk_add_f32 v[112:113], v[112:113], v[144:145]
	v_pk_add_f32 v[110:111], v[110:111], v[142:143]
	v_pk_add_f32 v[108:109], v[108:109], v[140:141]
	v_pk_add_f32 v[106:107], v[106:107], v[138:139]
	v_lshl_add_u64 v[114:115], v[168:169], 0, v[114:115]
	v_pk_mul_f32 v[112:113], v[112:113], v[188:189] op_sel_hi:[1,0]
	v_pk_mul_f32 v[110:111], v[110:111], v[188:189] op_sel_hi:[1,0]
	v_pk_mul_f32 v[116:117], v[108:109], v[188:189] op_sel_hi:[1,0]
	v_pk_mul_f32 v[108:109], v[106:107], v[188:189] op_sel_hi:[1,0]
	v_cvt_pk_bf16_f32 v106, v110, v111
	v_cvt_pk_bf16_f32 v107, v112, v113
	v_pk_add_f32 v[100:101], v[100:101], v[132:133]
	v_pk_add_f32 v[98:99], v[98:99], v[130:131]
	v_cvt_pk_bf16_f32 v108, v108, v109
	v_cvt_pk_bf16_f32 v109, v116, v117
	global_store_dwordx4 v[114:115], v[106:109], off
	v_pk_add_f32 v[104:105], v[104:105], v[136:137]
	v_pk_add_f32 v[102:103], v[102:103], v[134:135]
	v_pk_mul_f32 v[106:107], v[100:101], v[188:189] op_sel_hi:[1,0]
	v_pk_mul_f32 v[100:101], v[98:99], v[188:189] op_sel_hi:[1,0]
	v_pk_mul_f32 v[104:105], v[104:105], v[188:189] op_sel_hi:[1,0]
	v_pk_mul_f32 v[102:103], v[102:103], v[188:189] op_sel_hi:[1,0]
	s_nop 0
	v_cvt_pk_bf16_f32 v98, v102, v103
	v_cvt_pk_bf16_f32 v99, v104, v105
	v_cvt_pk_bf16_f32 v100, v100, v101
	v_cvt_pk_bf16_f32 v101, v106, v107
	global_store_dwordx4 v[114:115], v[98:101], off offset:256
.LBB0_2455:
	s_or_b64 exec, exec, s[18:19]
	s_nop 0
	v_add_u32_e32 v98, s24, v185
	v_cmp_lt_i32_e32 vcc, v98, v159
	s_and_saveexec_b64 s[18:19], vcc
	s_cbranch_execz .LBB0_2457
	v_ashrrev_i32_e32 v187, 31, v186
	v_lshlrev_b64 v[98:99], 11, v[186:187]
	v_pk_add_f32 v[96:97], v[96:97], v[144:145]
	v_pk_add_f32 v[94:95], v[94:95], v[142:143]
	v_pk_add_f32 v[92:93], v[92:93], v[140:141]
	v_pk_add_f32 v[90:91], v[90:91], v[138:139]
	v_lshl_add_u64 v[98:99], v[168:169], 0, v[98:99]
	v_pk_mul_f32 v[96:97], v[96:97], v[184:185] op_sel_hi:[1,0]
	v_pk_mul_f32 v[94:95], v[94:95], v[184:185] op_sel_hi:[1,0]
	v_pk_mul_f32 v[100:101], v[92:93], v[184:185] op_sel_hi:[1,0]
	v_pk_mul_f32 v[92:93], v[90:91], v[184:185] op_sel_hi:[1,0]
	v_cvt_pk_bf16_f32 v90, v94, v95
	v_cvt_pk_bf16_f32 v91, v96, v97
	v_pk_add_f32 v[84:85], v[84:85], v[132:133]
	v_pk_add_f32 v[82:83], v[82:83], v[130:131]
	v_cvt_pk_bf16_f32 v92, v92, v93
	v_cvt_pk_bf16_f32 v93, v100, v101
	global_store_dwordx4 v[98:99], v[90:93], off
	v_pk_add_f32 v[88:89], v[88:89], v[136:137]
	v_pk_add_f32 v[86:87], v[86:87], v[134:135]
	v_pk_mul_f32 v[90:91], v[84:85], v[184:185] op_sel_hi:[1,0]
	v_pk_mul_f32 v[84:85], v[82:83], v[184:185] op_sel_hi:[1,0]
	v_pk_mul_f32 v[88:89], v[88:89], v[184:185] op_sel_hi:[1,0]
	v_pk_mul_f32 v[86:87], v[86:87], v[184:185] op_sel_hi:[1,0]
	s_nop 0
	v_cvt_pk_bf16_f32 v82, v86, v87
	v_cvt_pk_bf16_f32 v83, v88, v89
	v_cvt_pk_bf16_f32 v84, v84, v85
	v_cvt_pk_bf16_f32 v85, v90, v91
	global_store_dwordx4 v[98:99], v[82:85], off offset:256
.LBB0_2457:
	s_or_b64 exec, exec, s[18:19]
	s_nop 0
	v_add_u32_e32 v82, s24, v189
	v_cmp_lt_i32_e32 vcc, v82, v159
	s_and_saveexec_b64 s[18:19], vcc
	s_cbranch_execz .LBB0_2463
	v_ashrrev_i32_e32 v183, 31, v182
	v_lshlrev_b64 v[82:83], 11, v[182:183]
	v_pk_add_f32 v[80:81], v[80:81], v[144:145]
	v_pk_add_f32 v[78:79], v[78:79], v[142:143]
	v_pk_add_f32 v[76:77], v[76:77], v[140:141]
	v_pk_add_f32 v[74:75], v[74:75], v[138:139]
	v_lshl_add_u64 v[82:83], v[168:169], 0, v[82:83]
	v_pk_mul_f32 v[80:81], v[80:81], v[180:181] op_sel_hi:[1,0]
	v_pk_mul_f32 v[78:79], v[78:79], v[180:181] op_sel_hi:[1,0]
	v_pk_mul_f32 v[84:85], v[76:77], v[180:181] op_sel_hi:[1,0]
	v_pk_mul_f32 v[76:77], v[74:75], v[180:181] op_sel_hi:[1,0]
	v_cvt_pk_bf16_f32 v74, v78, v79
	v_cvt_pk_bf16_f32 v75, v80, v81
	v_pk_add_f32 v[68:69], v[68:69], v[132:133]
	v_pk_add_f32 v[66:67], v[66:67], v[130:131]
	v_cvt_pk_bf16_f32 v76, v76, v77
	v_cvt_pk_bf16_f32 v77, v84, v85
	global_store_dwordx4 v[82:83], v[74:77], off
	v_pk_add_f32 v[72:73], v[72:73], v[136:137]
	v_pk_add_f32 v[70:71], v[70:71], v[134:135]
	v_pk_mul_f32 v[74:75], v[68:69], v[180:181] op_sel_hi:[1,0]
	v_pk_mul_f32 v[68:69], v[66:67], v[180:181] op_sel_hi:[1,0]
	v_pk_mul_f32 v[72:73], v[72:73], v[180:181] op_sel_hi:[1,0]
	v_pk_mul_f32 v[70:71], v[70:71], v[180:181] op_sel_hi:[1,0]
	s_nop 0
	v_cvt_pk_bf16_f32 v66, v70, v71
	v_cvt_pk_bf16_f32 v67, v72, v73
	v_cvt_pk_bf16_f32 v68, v68, v69
	v_cvt_pk_bf16_f32 v69, v74, v75
	global_store_dwordx4 v[82:83], v[66:69], off offset:256
	s_or_b64 exec, exec, s[18:19]
	v_cmp_lt_i32_e32 vcc, v179, v159
	s_and_saveexec_b64 s[18:19], vcc
	s_cbranch_execnz .LBB0_2464

; __device__ __forceinline__ unsigned cvt_pk_bf16(float lo, float hi) { unsigned r; asm volatile("v_cvt_pk_bf16_f32 %0, %1, %2" : "=v"(r) : "v"(lo), "v"(hi)); return r; }
;     __device__ __forceinline__ void operator()(const f32x4 (&acc)[2][2][4][2], const Unit& u, int wr, int wc, int fr, int fq) const {
;     ...
;             for (int m = 0; m < 4; ++m) { const int r = u.pm * 256 + ai * HALF + wr * 64 + m * 16 + fr;
;                 if (r < u.cnt) { const float gw = gwv[ai][m]; bf16* rowp = Y + (size_t)pr[ai][m] * 1024 + col0;
; #pragma unroll
;                     for (int bj = 0; bj < 2; ++bj) { const f32x4 v0 = (acc[ai][bj][m][0] + bv[bj][0]) * gw, v1 = (acc[ai][bj][m][1] + bv[bj][1]) * gw;
;                         u32x4 w; w.x = cvt_pk_bf16(v0[0], v0[1]); w.y = cvt_pk_bf16(v0[2], v0[3]); w.z = cvt_pk_bf16(v1[0], v1[1]); w.w = cvt_pk_bf16(v1[2], v1[3]);
;                         *(u32x4*)(rowp + bj * HALF) = w; } } }
.LBB0_2460:
	v_ashrrev_i32_e32 v177, 31, v176
	v_lshlrev_b64 v[50:51], 11, v[176:177]
	v_pk_add_f32 v[48:49], v[48:49], v[144:145]
	v_pk_add_f32 v[46:47], v[46:47], v[142:143]
	v_pk_add_f32 v[44:45], v[44:45], v[140:141]
	v_pk_add_f32 v[42:43], v[42:43], v[138:139]
	v_lshl_add_u64 v[50:51], v[168:169], 0, v[50:51]
	v_pk_mul_f32 v[48:49], v[48:49], v[172:173] op_sel_hi:[1,0]
	v_pk_mul_f32 v[46:47], v[46:47], v[172:173] op_sel_hi:[1,0]
	v_pk_mul_f32 v[52:53], v[44:45], v[172:173] op_sel_hi:[1,0]
	v_pk_mul_f32 v[44:45], v[42:43], v[172:173] op_sel_hi:[1,0]
	v_cvt_pk_bf16_f32 v42, v46, v47
	v_cvt_pk_bf16_f32 v43, v48, v49
	v_pk_add_f32 v[36:37], v[36:37], v[132:133]
	v_pk_add_f32 v[34:35], v[34:35], v[130:131]
	v_cvt_pk_bf16_f32 v44, v44, v45
	v_cvt_pk_bf16_f32 v45, v52, v53
	global_store_dwordx4 v[50:51], v[42:45], off
	v_pk_add_f32 v[40:41], v[40:41], v[136:137]
	v_pk_add_f32 v[38:39], v[38:39], v[134:135]
	v_pk_mul_f32 v[42:43], v[36:37], v[172:173] op_sel_hi:[1,0]
	v_pk_mul_f32 v[36:37], v[34:35], v[172:173] op_sel_hi:[1,0]
	v_pk_mul_f32 v[40:41], v[40:41], v[172:173] op_sel_hi:[1,0]
	v_pk_mul_f32 v[38:39], v[38:39], v[172:173] op_sel_hi:[1,0]
	s_nop 0
	v_cvt_pk_bf16_f32 v34, v38, v39
	v_cvt_pk_bf16_f32 v35, v40, v41
	v_cvt_pk_bf16_f32 v36, v36, v37
	v_cvt_pk_bf16_f32 v37, v42, v43
	global_store_dwordx4 v[50:51], v[34:37], off offset:256
	s_or_b64 exec, exec, s[18:19]
	v_cmp_lt_i32_e32 vcc, v171, v159
	s_and_saveexec_b64 s[18:19], vcc
	s_cbranch_execnz .LBB0_2466

; __device__ __forceinline__ unsigned cvt_pk_bf16(float lo, float hi) { unsigned r; asm volatile("v_cvt_pk_bf16_f32 %0, %1, %2" : "=v"(r) : "v"(lo), "v"(hi)); return r; }
;     __device__ __forceinline__ void operator()(const f32x4 (&acc)[2][2][4][2], const Unit& u, int wr, int wc, int fr, int fq) const {
;     ...
;             for (int m = 0; m < 4; ++m) { const int r = u.pm * 256 + ai * HALF + wr * 64 + m * 16 + fr;
;                 if (r < u.cnt) { const float gw = gwv[ai][m]; bf16* rowp = Y + (size_t)pr[ai][m] * 1024 + col0;
; #pragma unroll
;                     for (int bj = 0; bj < 2; ++bj) { const f32x4 v0 = (acc[ai][bj][m][0] + bv[bj][0]) * gw, v1 = (acc[ai][bj][m][1] + bv[bj][1]) * gw;
;                         u32x4 w; w.x = cvt_pk_bf16(v0[0], v0[1]); w.y = cvt_pk_bf16(v0[2], v0[3]); w.z = cvt_pk_bf16(v1[0], v1[1]); w.w = cvt_pk_bf16(v1[2], v1[3]);
;                         *(u32x4*)(rowp + bj * HALF) = w; } } }
.LBB0_2462:
	v_ashrrev_i32_e32 v167, 31, v166
	v_lshlrev_b64 v[18:19], 11, v[166:167]
	v_pk_add_f32 v[16:17], v[16:17], v[144:145]
	v_pk_add_f32 v[14:15], v[14:15], v[142:143]
	v_pk_add_f32 v[12:13], v[12:13], v[140:141]
	v_pk_add_f32 v[10:11], v[10:11], v[138:139]
	v_lshl_add_u64 v[18:19], v[168:169], 0, v[18:19]
	v_pk_mul_f32 v[16:17], v[16:17], v[158:159] op_sel_hi:[1,0]
	v_pk_mul_f32 v[14:15], v[14:15], v[158:159] op_sel_hi:[1,0]
	v_pk_mul_f32 v[20:21], v[12:13], v[158:159] op_sel_hi:[1,0]
	v_pk_mul_f32 v[12:13], v[10:11], v[158:159] op_sel_hi:[1,0]
	v_cvt_pk_bf16_f32 v10, v14, v15
	v_cvt_pk_bf16_f32 v11, v16, v17
	v_pk_add_f32 v[4:5], v[4:5], v[132:133]
	v_pk_add_f32 v[2:3], v[2:3], v[130:131]
	v_cvt_pk_bf16_f32 v12, v12, v13
	v_cvt_pk_bf16_f32 v13, v20, v21
	global_store_dwordx4 v[18:19], v[10:13], off
	v_pk_add_f32 v[8:9], v[8:9], v[136:137]
	v_pk_add_f32 v[6:7], v[6:7], v[134:135]
	v_pk_mul_f32 v[10:11], v[4:5], v[158:159] op_sel_hi:[1,0]
	v_pk_mul_f32 v[4:5], v[2:3], v[158:159] op_sel_hi:[1,0]
	v_pk_mul_f32 v[8:9], v[8:9], v[158:159] op_sel_hi:[1,0]
	v_pk_mul_f32 v[6:7], v[6:7], v[158:159] op_sel_hi:[1,0]
	s_nop 0
	v_cvt_pk_bf16_f32 v2, v6, v7
	v_cvt_pk_bf16_f32 v3, v8, v9
	v_cvt_pk_bf16_f32 v4, v4, v5
	v_cvt_pk_bf16_f32 v5, v10, v11
	global_store_dwordx4 v[18:19], v[2:5], off offset:256
	s_or_b64 exec, exec, s[18:19]
	s_andn2_b64 vcc, exec, s[4:5]
	s_mov_b64 s[4:5], -1
	s_cbranch_vccnz .LBB0_2442
	s_branch .LBB0_2468

; __device__ __forceinline__ unsigned cvt_pk_bf16(float lo, float hi) { unsigned r; asm volatile("v_cvt_pk_bf16_f32 %0, %1, %2" : "=v"(r) : "v"(lo), "v"(hi)); return r; }
;     __device__ __forceinline__ void operator()(const f32x4 (&acc)[2][2][4][2], const Unit& u, int wr, int wc, int fr, int fq) const {
;     ...
;             for (int m = 0; m < 4; ++m) { const int r = u.pm * 256 + ai * HALF + wr * 64 + m * 16 + fr;
;                 if (r < u.cnt) { const float gw = gwv[ai][m]; bf16* rowp = Y + (size_t)pr[ai][m] * 1024 + col0;
; #pragma unroll
;                     for (int bj = 0; bj < 2; ++bj) { const f32x4 v0 = (acc[ai][bj][m][0] + bv[bj][0]) * gw, v1 = (acc[ai][bj][m][1] + bv[bj][1]) * gw;
;                         u32x4 w; w.x = cvt_pk_bf16(v0[0], v0[1]); w.y = cvt_pk_bf16(v0[2], v0[3]); w.z = cvt_pk_bf16(v1[0], v1[1]); w.w = cvt_pk_bf16(v1[2], v1[3]);
;                         *(u32x4*)(rowp + bj * HALF) = w; } } }
.LBB0_2464:
	v_ashrrev_i32_e32 v179, 31, v178
	v_lshlrev_b64 v[66:67], 11, v[178:179]
	v_pk_add_f32 v[64:65], v[64:65], v[144:145]
	v_pk_add_f32 v[62:63], v[62:63], v[142:143]
	v_pk_add_f32 v[60:61], v[60:61], v[140:141]
	v_pk_add_f32 v[58:59], v[58:59], v[138:139]
	v_lshl_add_u64 v[66:67], v[168:169], 0, v[66:67]
	v_pk_mul_f32 v[64:65], v[64:65], v[174:175] op_sel_hi:[1,0]
	v_pk_mul_f32 v[62:63], v[62:63], v[174:175] op_sel_hi:[1,0]
	v_pk_mul_f32 v[68:69], v[60:61], v[174:175] op_sel_hi:[1,0]
	v_pk_mul_f32 v[60:61], v[58:59], v[174:175] op_sel_hi:[1,0]
	v_cvt_pk_bf16_f32 v58, v62, v63
	v_cvt_pk_bf16_f32 v59, v64, v65
	v_pk_add_f32 v[52:53], v[52:53], v[132:133]
	v_pk_add_f32 v[50:51], v[50:51], v[130:131]
	v_cvt_pk_bf16_f32 v60, v60, v61
	v_cvt_pk_bf16_f32 v61, v68, v69
	global_store_dwordx4 v[66:67], v[58:61], off
	v_pk_add_f32 v[56:57], v[56:57], v[136:137]
	v_pk_add_f32 v[54:55], v[54:55], v[134:135]
	v_pk_mul_f32 v[58:59], v[52:53], v[174:175] op_sel_hi:[1,0]
	v_pk_mul_f32 v[52:53], v[50:51], v[174:175] op_sel_hi:[1,0]
	v_pk_mul_f32 v[56:57], v[56:57], v[174:175] op_sel_hi:[1,0]
	v_pk_mul_f32 v[54:55], v[54:55], v[174:175] op_sel_hi:[1,0]
	s_nop 0
	v_cvt_pk_bf16_f32 v50, v54, v55
	v_cvt_pk_bf16_f32 v51, v56, v57
	v_cvt_pk_bf16_f32 v52, v52, v53
	v_cvt_pk_bf16_f32 v53, v58, v59
	global_store_dwordx4 v[66:67], v[50:53], off offset:256
	s_or_b64 exec, exec, s[18:19]
	v_cmp_lt_i32_e32 vcc, v177, v159
	s_and_saveexec_b64 s[18:19], vcc
	s_cbranch_execnz .LBB0_2460

; __device__ __forceinline__ unsigned cvt_pk_bf16(float lo, float hi) { unsigned r; asm volatile("v_cvt_pk_bf16_f32 %0, %1, %2" : "=v"(r) : "v"(lo), "v"(hi)); return r; }
;     __device__ __forceinline__ void operator()(const f32x4 (&acc)[2][2][4][2], const Unit& u, int wr, int wc, int fr, int fq) const {
;     ...
;             for (int m = 0; m < 4; ++m) { const int r = u.pm * 256 + ai * HALF + wr * 64 + m * 16 + fr;
;                 if (r < u.cnt) { const float gw = gwv[ai][m]; bf16* rowp = Y + (size_t)pr[ai][m] * 1024 + col0;
; #pragma unroll
;                     for (int bj = 0; bj < 2; ++bj) { const f32x4 v0 = (acc[ai][bj][m][0] + bv[bj][0]) * gw, v1 = (acc[ai][bj][m][1] + bv[bj][1]) * gw;
;                         u32x4 w; w.x = cvt_pk_bf16(v0[0], v0[1]); w.y = cvt_pk_bf16(v0[2], v0[3]); w.z = cvt_pk_bf16(v1[0], v1[1]); w.w = cvt_pk_bf16(v1[2], v1[3]);
;                         *(u32x4*)(rowp + bj * HALF) = w; } } }
.LBB0_2466:
	v_ashrrev_i32_e32 v171, 31, v170
	v_lshlrev_b64 v[34:35], 11, v[170:171]
	v_pk_add_f32 v[32:33], v[32:33], v[144:145]
	v_pk_add_f32 v[30:31], v[30:31], v[142:143]
	v_pk_add_f32 v[28:29], v[28:29], v[140:141]
	v_pk_add_f32 v[26:27], v[26:27], v[138:139]
	v_lshl_add_u64 v[34:35], v[168:169], 0, v[34:35]
	v_pk_mul_f32 v[32:33], v[32:33], v[164:165] op_sel_hi:[1,0]
	v_pk_mul_f32 v[30:31], v[30:31], v[164:165] op_sel_hi:[1,0]
	v_pk_mul_f32 v[36:37], v[28:29], v[164:165] op_sel_hi:[1,0]
	v_pk_mul_f32 v[28:29], v[26:27], v[164:165] op_sel_hi:[1,0]
	v_cvt_pk_bf16_f32 v26, v30, v31
	v_cvt_pk_bf16_f32 v27, v32, v33
	v_pk_add_f32 v[20:21], v[20:21], v[132:133]
	v_pk_add_f32 v[18:19], v[18:19], v[130:131]
	v_cvt_pk_bf16_f32 v28, v28, v29
	v_cvt_pk_bf16_f32 v29, v36, v37
	global_store_dwordx4 v[34:35], v[26:29], off
	v_pk_add_f32 v[24:25], v[24:25], v[136:137]
	v_pk_add_f32 v[22:23], v[22:23], v[134:135]
	v_pk_mul_f32 v[26:27], v[20:21], v[164:165] op_sel_hi:[1,0]
	v_pk_mul_f32 v[20:21], v[18:19], v[164:165] op_sel_hi:[1,0]
	v_pk_mul_f32 v[24:25], v[24:25], v[164:165] op_sel_hi:[1,0]
	v_pk_mul_f32 v[22:23], v[22:23], v[164:165] op_sel_hi:[1,0]
	s_nop 0
	v_cvt_pk_bf16_f32 v18, v22, v23
	v_cvt_pk_bf16_f32 v19, v24, v25
	v_cvt_pk_bf16_f32 v20, v20, v21
	v_cvt_pk_bf16_f32 v21, v26, v27
	global_store_dwordx4 v[34:35], v[18:21], off offset:256
	s_or_b64 exec, exec, s[18:19]
	v_cmp_lt_i32_e32 vcc, v167, v159
	s_and_saveexec_b64 s[18:19], vcc
	s_cbranch_execnz .LBB0_2462
